# code placement scan: both attention main loops at byte phase 32 mod 64
# speedup vs baseline: 1.0052x; 1.0052x over previous
.LBB0_259:
	s_add_i32 s21, s21, 1
	s_cmp_eq_u32 s21, 4
	s_cbranch_scc1 .LBB0_349
	s_nop 0
	s_nop 0
	s_nop 0
	s_nop 0
.LBB0_260:
	s_lshr_b32 s84, s21, 1
	s_bitcmp0_b32 s21, 0
	s_cselect_b32 s82, s49, s48
	s_lshl_b32 s0, s84, 7
	s_add_u32 s3, s52, s0
	s_addc_u32 s33, s53, 0
	s_add_u32 s39, s54, s0
	v_mov_b32_e32 v36, v0
	s_mov_b32 s38, s82
	s_mov_b32 s0, s4
	s_addc_u32 s43, s55, 0
	s_ashr_i32 s1, s0, 31
	v_readfirstlane_b32 s2, v36
	s_lshl_b64 s[34:35], s[0:1], 14
	s_lshl_b32 s1, s38, 8
	s_ashr_i32 s83, s2, 6
	s_ashr_i32 s36, s1, 31
	s_add_u32 s34, s34, s1
	s_addc_u32 s35, s35, s36
	s_lshl_b32 s46, s83, 5
	s_ashr_i32 s36, s46, 31
	s_add_u32 s34, s34, s46
	s_addc_u32 s35, s35, s36
	s_mul_i32 s36, s35, 0x1200
	s_mul_hi_u32 s37, s34, 0x1200
	s_add_i32 s37, s37, s36
	s_mul_i32 s36, s34, 0x1200
	s_add_u32 s36, s3, s36
	s_addc_u32 s37, s33, s37
	s_mul_hi_i32 s3, s0, 0x4800000
	s_mul_i32 s0, s0, 0x4800000
	v_and_b32_e32 v230, 63, v36
	s_add_u32 s42, s39, s0
	s_addc_u32 s43, s43, s3
	v_mul_u32_u24_e32 v2, 0x900, v230
	s_add_u32 s44, s62, s0
	v_lshlrev_b32_e32 v2, 1, v2
	s_addc_u32 s45, s63, s3
	v_lshl_add_u64 v[4:5], s[42:43], 0, v[2:3]
	s_lshl_b32 s42, s83, 3
	s_lshl_b32 s0, s83, 4
	v_bfe_u32 v2, v36, 2, 4
	s_ashr_i32 s43, s42, 31
	v_and_or_b32 v2, s0, 48, v2
	s_ashr_i32 s0, s2, 3
	v_lshl_add_u64 v[216:217], s[42:43], 1, v[4:5]
	s_and_b32 s42, s0, 0xffffffe0
	v_mul_u32_u24_e32 v2, 0x900, v2
	s_ashr_i32 s43, s42, 31
	s_lshl_b32 s0, s83, 10
	v_lshlrev_b32_e32 v2, 1, v2
	v_lshlrev_b32_e32 v232, 3, v36
	s_cmp_lg_u32 0, -1
	v_lshl_add_u64 v[4:5], s[44:45], 0, v[2:3]
	v_and_b32_e32 v233, 24, v232
	s_cselect_b32 s3, 0, 0
	v_and_b32_e32 v231, 31, v36
	v_lshl_add_u64 v[4:5], s[42:43], 1, v[4:5]
	v_lshlrev_b32_e32 v2, 1, v233
	s_add_i32 s76, s0, s3
	s_mov_b32 m0, s76
	s_nop 0
	global_load_lds_dwordx4 v[216:217], off
	v_lshl_add_u64 v[218:219], v[4:5], 0, v[2:3]
	s_add_i32 s77, s76, 0x6000
	s_mov_b32 m0, s77
	s_nop 0
	global_load_lds_dwordx4 v[218:219], off
	s_mov_b64 s[42:43], 0x80
	v_mul_u32_u24_e32 v2, 0x900, v231
	v_bfe_u32 v229, v36, 5, 1
	v_lshl_add_u64 v[220:221], v[218:219], 0, s[42:43]
	s_add_i32 s3, s76, 0x8000
	s_mov_b32 m0, s3
	s_nop 0
	global_load_lds_dwordx4 v[220:221], off
	v_lshlrev_b32_e32 v2, 1, v2
	v_lshl_add_u64 v[4:5], v[216:217], 0, s[26:27]
	s_add_i32 s3, s76, 0x2000
	s_mov_b32 m0, s3
	s_nop 0
	global_load_lds_dwordx4 v[4:5], off
	v_lshl_or_b32 v2, v229, 4, v2
	global_load_dwordx4 v[154:157], v2, s[36:37]
	global_load_dwordx4 v[150:153], v2, s[36:37] offset:32
	global_load_dwordx4 v[146:149], v2, s[36:37] offset:64
	global_load_dwordx4 v[142:145], v2, s[36:37] offset:96
	s_mov_b64 s[36:37], 0x48080
	v_lshlrev_b32_e32 v2, 10, v229
	v_lshlrev_b32_e32 v4, 4, v231
	v_add3_u32 v240, 0, v2, v4
	v_lshl_add_u64 v[4:5], v[216:217], 0, s[28:29]
	s_add_i32 s3, s76, 0x4000
	v_lshl_add_u64 v[8:9], v[218:219], 0, s[36:37]
	s_mov_b32 m0, s3
	s_nop 0
	global_load_lds_dwordx4 v[4:5], off
	s_add_i32 s33, s76, 0xa000
	v_lshl_add_u64 v[6:7], v[218:219], 0, s[26:27]
	s_mov_b32 m0, s33
	s_nop 0
	global_load_lds_dwordx4 v[6:7], off
	s_add_i32 s39, s76, 0xc000
	s_mov_b32 m0, s39
	s_nop 0
	global_load_lds_dwordx4 v[8:9], off
	s_waitcnt vmcnt(6) lgkmcnt(0)
	s_barrier
	ds_read_b128 v[4:7], v240
	ds_read_b128 v[8:11], v240 offset:512
	ds_read_b128 v[38:41], v240 offset:2048
	ds_read_b128 v[42:45], v240 offset:2560
	s_add_i32 s3, s1, 0x100
	s_ashr_i32 s85, s3, 6
	v_lshlrev_b32_e32 v239, 2, v229
	v_or_b32_e32 v238, s46, v231
	s_cmp_gt_i32 s85, 4
	s_waitcnt vmcnt(3) lgkmcnt(3)
	v_mfma_f32_32x32x16_bf16 v[20:35], v[4:7], v[154:157], 0
	s_waitcnt lgkmcnt(2)
	v_mfma_f32_32x32x16_bf16 v[4:19], v[8:11], v[154:157], 0
	s_waitcnt vmcnt(2) lgkmcnt(1)
	v_mfma_f32_32x32x16_bf16 v[20:35], v[38:41], v[150:153], v[20:35]
	s_waitcnt lgkmcnt(0)
	v_mfma_f32_32x32x16_bf16 v[4:19], v[42:45], v[150:153], v[4:19]
	ds_read_b128 v[38:41], v240 offset:4096
	ds_read_b128 v[42:45], v240 offset:4608
	s_waitcnt vmcnt(1) lgkmcnt(1)
	v_mfma_f32_32x32x16_bf16 v[20:35], v[38:41], v[146:149], v[20:35]
	s_waitcnt lgkmcnt(0)
	v_mfma_f32_32x32x16_bf16 v[4:19], v[42:45], v[146:149], v[4:19]
	ds_read_b128 v[38:41], v240 offset:6144
	ds_read_b128 v[42:45], v240 offset:6656
	s_waitcnt vmcnt(0) lgkmcnt(1)
	v_mfma_f32_32x32x16_bf16 v[20:35], v[38:41], v[142:145], v[20:35]
	s_waitcnt lgkmcnt(0)
	v_mfma_f32_32x32x16_bf16 v[4:19], v[42:45], v[142:145], v[4:19]
	s_nop 15
	s_nop 7
	s_cbranch_scc1 .LBB0_262
	v_subrev_u32_e32 v2, s1, v239
	v_or_b32_e32 v37, 32, v2
	v_cmp_le_i32_e32 vcc, v37, v238
	v_or_b32_e32 v37, 33, v2
	s_nop 6
	v_cndmask_b32_e32 v4, v227, v4, vcc
	v_cmp_lt_i32_e32 vcc, v2, v238
	s_nop 1
	v_cndmask_b32_e32 v21, v227, v21, vcc
	v_cmp_le_i32_e32 vcc, v2, v238
	s_nop 1
	v_cndmask_b32_e32 v20, v227, v20, vcc
	v_cmp_le_i32_e32 vcc, v37, v238
	v_or_b32_e32 v37, 2, v2
	s_nop 0
	v_cndmask_b32_e32 v5, v227, v5, vcc
	v_cmp_le_i32_e32 vcc, v37, v238
	v_or_b32_e32 v37, 34, v2
	s_nop 0
	v_cndmask_b32_e32 v22, v227, v22, vcc
	v_cmp_le_i32_e32 vcc, v37, v238
	v_or_b32_e32 v37, 3, v2
	s_nop 0
	v_cndmask_b32_e32 v6, v227, v6, vcc
	v_cmp_le_i32_e32 vcc, v37, v238
	v_or_b32_e32 v37, 35, v2
	s_nop 0
	v_cndmask_b32_e32 v23, v227, v23, vcc
	v_cmp_le_i32_e32 vcc, v37, v238
	v_or_b32_e32 v37, 8, v2
	s_nop 0
	v_cndmask_b32_e32 v7, v227, v7, vcc
	v_cmp_le_i32_e32 vcc, v37, v238
	v_or_b32_e32 v37, 40, v2
	s_nop 0
	v_cndmask_b32_e32 v24, v227, v24, vcc
	v_cmp_le_i32_e32 vcc, v37, v238
	v_or_b32_e32 v37, 9, v2
	s_nop 0
	v_cndmask_b32_e32 v8, v227, v8, vcc
	v_cmp_le_i32_e32 vcc, v37, v238
	v_or_b32_e32 v37, 41, v2
	s_nop 0
	v_cndmask_b32_e32 v25, v227, v25, vcc
	v_cmp_le_i32_e32 vcc, v37, v238
	v_or_b32_e32 v37, 10, v2
	s_nop 0
	v_cndmask_b32_e32 v9, v227, v9, vcc
	v_cmp_le_i32_e32 vcc, v37, v238
	v_or_b32_e32 v37, 42, v2
	s_nop 0
	v_cndmask_b32_e32 v26, v227, v26, vcc
	v_cmp_le_i32_e32 vcc, v37, v238
	v_or_b32_e32 v37, 11, v2
	s_nop 0
	v_cndmask_b32_e32 v10, v227, v10, vcc
	v_cmp_le_i32_e32 vcc, v37, v238
	v_or_b32_e32 v37, 43, v2
	s_nop 0
	v_cndmask_b32_e32 v27, v227, v27, vcc
	v_cmp_le_i32_e32 vcc, v37, v238
	v_or_b32_e32 v37, 16, v2
	s_nop 0
	v_cndmask_b32_e32 v11, v227, v11, vcc
	v_cmp_le_i32_e32 vcc, v37, v238
	v_or_b32_e32 v37, 48, v2
	s_nop 0
	v_cndmask_b32_e32 v28, v227, v28, vcc
	v_cmp_le_i32_e32 vcc, v37, v238
	v_or_b32_e32 v37, 17, v2
	s_nop 0
	v_cndmask_b32_e32 v12, v227, v12, vcc
	v_cmp_le_i32_e32 vcc, v37, v238
	v_or_b32_e32 v37, 49, v2
	s_nop 0
	v_cndmask_b32_e32 v29, v227, v29, vcc
	v_cmp_le_i32_e32 vcc, v37, v238
	v_or_b32_e32 v37, 18, v2
	s_nop 0
	v_cndmask_b32_e32 v13, v227, v13, vcc
	v_cmp_le_i32_e32 vcc, v37, v238
	v_or_b32_e32 v37, 50, v2
	s_nop 0
	v_cndmask_b32_e32 v30, v227, v30, vcc
	v_cmp_le_i32_e32 vcc, v37, v238
	v_or_b32_e32 v37, 19, v2
	s_nop 0
	v_cndmask_b32_e32 v14, v227, v14, vcc
	v_cmp_le_i32_e32 vcc, v37, v238
	v_or_b32_e32 v37, 51, v2
	s_nop 0
	v_cndmask_b32_e32 v31, v227, v31, vcc
	v_cmp_le_i32_e32 vcc, v37, v238
	v_or_b32_e32 v37, 24, v2
	s_nop 0
	v_cndmask_b32_e32 v15, v227, v15, vcc
	v_cmp_le_i32_e32 vcc, v37, v238
	v_or_b32_e32 v37, 56, v2
	s_nop 0
	v_cndmask_b32_e32 v32, v227, v32, vcc
	v_cmp_le_i32_e32 vcc, v37, v238
	v_or_b32_e32 v37, 25, v2
	s_nop 0
	v_cndmask_b32_e32 v16, v227, v16, vcc
	v_cmp_le_i32_e32 vcc, v37, v238
	v_or_b32_e32 v37, 57, v2
	s_nop 0
	v_cndmask_b32_e32 v33, v227, v33, vcc
	v_cmp_le_i32_e32 vcc, v37, v238
	v_or_b32_e32 v37, 26, v2
	s_nop 0
	v_cndmask_b32_e32 v17, v227, v17, vcc
	v_cmp_le_i32_e32 vcc, v37, v238
	v_or_b32_e32 v37, 58, v2
	s_nop 0
	v_cndmask_b32_e32 v34, v227, v34, vcc
	v_cmp_le_i32_e32 vcc, v37, v238
	v_or_b32_e32 v37, 27, v2
	v_or_b32_e32 v2, 59, v2
	v_cndmask_b32_e32 v18, v227, v18, vcc
	v_cmp_le_i32_e32 vcc, v37, v238
	s_nop 1
	v_cndmask_b32_e32 v35, v227, v35, vcc
	v_cmp_le_i32_e32 vcc, v2, v238
	s_nop 1
	v_cndmask_b32_e32 v19, v227, v19, vcc

.LBB0_346:
	v_max_f32_e32 v16, v16, v16
	v_max_f32_e32 v17, 0, v16
	v_exp_f32_e64 v16, -v17
	v_cmp_gt_u32_e32 vcc, 32, v230
	s_and_saveexec_b64 s[2:3], vcc
	ds_write_b32 v235, v16
	s_or_b64 exec, exec, s[2:3]
	v_sub_f32_e32 v113, v113, v17
	v_sub_f32_e32 v112, v112, v17
	v_sub_f32_e32 v111, v111, v17
	v_sub_f32_e32 v110, v110, v17
	v_sub_f32_e32 v109, v109, v17
	v_sub_f32_e32 v108, v108, v17
	v_sub_f32_e32 v107, v107, v17
	v_sub_f32_e32 v106, v106, v17
	v_sub_f32_e32 v105, v105, v17
	v_sub_f32_e32 v104, v104, v17
	v_sub_f32_e32 v103, v103, v17
	v_sub_f32_e32 v102, v102, v17
	v_sub_f32_e32 v101, v101, v17
	v_sub_f32_e32 v100, v100, v17
	v_sub_f32_e32 v99, v99, v17
	v_sub_f32_e32 v98, v98, v17
	v_sub_f32_e32 v97, v97, v17
	v_sub_f32_e32 v96, v96, v17
	v_sub_f32_e32 v95, v95, v17
	v_sub_f32_e32 v94, v94, v17
	v_sub_f32_e32 v93, v93, v17
	v_sub_f32_e32 v92, v92, v17
	v_sub_f32_e32 v91, v91, v17
	v_sub_f32_e32 v90, v90, v17
	v_sub_f32_e32 v89, v89, v17
	v_sub_f32_e32 v88, v88, v17
	v_sub_f32_e32 v87, v87, v17
	v_sub_f32_e32 v86, v86, v17
	v_sub_f32_e32 v85, v85, v17
	v_sub_f32_e32 v84, v84, v17
	v_sub_f32_e32 v83, v83, v17
	v_sub_f32_e32 v82, v82, v17
	v_mul_f32_e32 v243, v243, v16
	s_branch .LBB0_340
	s_nop 0
	s_nop 0
	s_nop 0
	s_nop 0
	s_nop 0
	s_nop 0
	s_nop 0
	s_nop 0
	s_nop 0
	s_nop 0
	s_nop 0
	s_nop 0

.LBB0_872:
	s_add_i32 s21, s21, 1
	s_cmp_eq_u32 s21, 4
	s_cbranch_scc1 .LBB0_962
	s_nop 0
	s_nop 0
	s_nop 0
.LBB0_873:
	s_lshr_b32 s42, s21, 1
	s_bitcmp0_b32 s21, 0
	s_cselect_b32 s63, s50, s47
	s_lshl_b32 s0, s42, 7
	s_add_u32 s3, s51, s0
	s_addc_u32 s29, s52, 0
	s_add_u32 s31, s53, s0
	v_mov_b32_e32 v36, v0
	s_mov_b32 s30, s63
	s_mov_b32 s0, s4
	s_addc_u32 s35, s55, 0
	s_ashr_i32 s1, s0, 31
	v_readfirstlane_b32 s2, v36
	s_lshl_b64 s[26:27], s[0:1], 14
	s_lshl_b32 s1, s30, 8
	s_ashr_i32 s33, s2, 6
	s_ashr_i32 s28, s1, 31
	s_add_u32 s26, s26, s1
	s_addc_u32 s27, s27, s28
	s_lshl_b32 s38, s33, 5
	s_ashr_i32 s28, s38, 31
	s_add_u32 s26, s26, s38
	s_addc_u32 s27, s27, s28
	s_mul_i32 s28, s27, 0x1200
	s_mul_hi_u32 s34, s26, 0x1200
	s_add_i32 s34, s34, s28
	s_mul_i32 s28, s26, 0x1200
	s_add_u32 s28, s3, s28
	s_addc_u32 s29, s29, s34
	s_mul_hi_i32 s3, s0, 0x4800000
	s_mul_i32 s0, s0, 0x4800000
	v_and_b32_e32 v230, 63, v36
	s_add_u32 s34, s31, s0
	s_addc_u32 s35, s35, s3
	v_mul_u32_u24_e32 v2, 0x900, v230
	s_add_u32 s36, s56, s0
	v_lshlrev_b32_e32 v2, 1, v2
	s_addc_u32 s37, s57, s3
	v_lshl_add_u64 v[4:5], s[34:35], 0, v[2:3]
	s_lshl_b32 s34, s33, 3
	s_lshl_b32 s0, s33, 4
	v_bfe_u32 v2, v36, 2, 4
	s_ashr_i32 s35, s34, 31
	v_and_or_b32 v2, s0, 48, v2
	s_ashr_i32 s0, s2, 3
	v_lshl_add_u64 v[216:217], s[34:35], 1, v[4:5]
	s_and_b32 s34, s0, 0xffffffe0
	v_mul_u32_u24_e32 v2, 0x900, v2
	s_ashr_i32 s35, s34, 31
	s_lshl_b32 s0, s33, 10
	v_lshlrev_b32_e32 v2, 1, v2
	v_lshlrev_b32_e32 v232, 3, v36
	s_cmp_lg_u32 0, -1
	v_lshl_add_u64 v[4:5], s[36:37], 0, v[2:3]
	v_and_b32_e32 v233, 24, v232
	s_cselect_b32 s3, 0, 0
	v_and_b32_e32 v231, 31, v36
	v_lshl_add_u64 v[4:5], s[34:35], 1, v[4:5]
	v_lshlrev_b32_e32 v2, 1, v233
	s_add_i32 s76, s0, s3
	s_mov_b32 m0, s76
	s_nop 0
	global_load_lds_dwordx4 v[216:217], off
	v_lshl_add_u64 v[218:219], v[4:5], 0, v[2:3]
	s_add_i32 s77, s76, 0x6000
	s_mov_b32 m0, s77
	s_nop 0
	global_load_lds_dwordx4 v[218:219], off
	s_mov_b64 s[34:35], 0x80
	v_mul_u32_u24_e32 v2, 0x900, v231
	v_bfe_u32 v229, v36, 5, 1
	v_lshl_add_u64 v[220:221], v[218:219], 0, s[34:35]
	s_add_i32 s3, s76, 0x8000
	s_mov_b32 m0, s3
	s_nop 0
	global_load_lds_dwordx4 v[220:221], off
	v_lshlrev_b32_e32 v2, 1, v2
	v_lshl_add_u64 v[4:5], v[216:217], 0, s[18:19]
	s_add_i32 s3, s76, 0x2000
	s_mov_b32 m0, s3
	s_nop 0
	global_load_lds_dwordx4 v[4:5], off
	v_lshl_or_b32 v2, v229, 4, v2
	global_load_dwordx4 v[154:157], v2, s[28:29]
	global_load_dwordx4 v[150:153], v2, s[28:29] offset:32
	global_load_dwordx4 v[146:149], v2, s[28:29] offset:64
	global_load_dwordx4 v[142:145], v2, s[28:29] offset:96
	s_mov_b64 s[28:29], 0x48080
	v_lshlrev_b32_e32 v2, 10, v229
	v_lshlrev_b32_e32 v4, 4, v231
	v_add3_u32 v240, 0, v2, v4
	v_lshl_add_u64 v[4:5], v[216:217], 0, s[22:23]
	s_add_i32 s3, s76, 0x4000
	v_lshl_add_u64 v[8:9], v[218:219], 0, s[28:29]
	s_mov_b32 m0, s3
	s_nop 0
	global_load_lds_dwordx4 v[4:5], off
	s_add_i32 s31, s76, 0xa000
	v_lshl_add_u64 v[6:7], v[218:219], 0, s[18:19]
	s_mov_b32 m0, s31
	s_nop 0
	global_load_lds_dwordx4 v[6:7], off
	s_add_i32 s34, s76, 0xc000
	s_mov_b32 m0, s34
	s_nop 0
	global_load_lds_dwordx4 v[8:9], off
	s_waitcnt vmcnt(6) lgkmcnt(0)
	s_barrier
	ds_read_b128 v[4:7], v240
	ds_read_b128 v[8:11], v240 offset:512
	ds_read_b128 v[38:41], v240 offset:2048
	ds_read_b128 v[42:45], v240 offset:2560
	s_add_i32 s3, s1, 0x100
	s_ashr_i32 s79, s3, 6
	v_lshlrev_b32_e32 v239, 2, v229
	v_or_b32_e32 v238, s38, v231
	s_cmp_gt_i32 s79, 4
	s_waitcnt vmcnt(3) lgkmcnt(3)
	v_mfma_f32_32x32x16_bf16 v[20:35], v[4:7], v[154:157], 0
	s_waitcnt lgkmcnt(2)
	v_mfma_f32_32x32x16_bf16 v[4:19], v[8:11], v[154:157], 0
	s_waitcnt vmcnt(2) lgkmcnt(1)
	v_mfma_f32_32x32x16_bf16 v[20:35], v[38:41], v[150:153], v[20:35]
	s_waitcnt lgkmcnt(0)
	v_mfma_f32_32x32x16_bf16 v[4:19], v[42:45], v[150:153], v[4:19]
	ds_read_b128 v[38:41], v240 offset:4096
	ds_read_b128 v[42:45], v240 offset:4608
	s_waitcnt vmcnt(1) lgkmcnt(1)
	v_mfma_f32_32x32x16_bf16 v[20:35], v[38:41], v[146:149], v[20:35]
	s_waitcnt lgkmcnt(0)
	v_mfma_f32_32x32x16_bf16 v[4:19], v[42:45], v[146:149], v[4:19]
	ds_read_b128 v[38:41], v240 offset:6144
	ds_read_b128 v[42:45], v240 offset:6656
	s_waitcnt vmcnt(0) lgkmcnt(1)
	v_mfma_f32_32x32x16_bf16 v[20:35], v[38:41], v[142:145], v[20:35]
	s_waitcnt lgkmcnt(0)
	v_mfma_f32_32x32x16_bf16 v[4:19], v[42:45], v[142:145], v[4:19]
	s_nop 15
	s_nop 7
	s_cbranch_scc1 .LBB0_875
	v_subrev_u32_e32 v2, s1, v239
	v_or_b32_e32 v37, 32, v2
	v_cmp_le_i32_e32 vcc, v37, v238
	v_or_b32_e32 v37, 33, v2
	s_nop 6
	v_cndmask_b32_e32 v4, v227, v4, vcc
	v_cmp_lt_i32_e32 vcc, v2, v238
	s_nop 1
	v_cndmask_b32_e32 v21, v227, v21, vcc
	v_cmp_le_i32_e32 vcc, v2, v238
	s_nop 1
	v_cndmask_b32_e32 v20, v227, v20, vcc
	v_cmp_le_i32_e32 vcc, v37, v238
	v_or_b32_e32 v37, 2, v2
	s_nop 0
	v_cndmask_b32_e32 v5, v227, v5, vcc
	v_cmp_le_i32_e32 vcc, v37, v238
	v_or_b32_e32 v37, 34, v2
	s_nop 0
	v_cndmask_b32_e32 v22, v227, v22, vcc
	v_cmp_le_i32_e32 vcc, v37, v238
	v_or_b32_e32 v37, 3, v2
	s_nop 0
	v_cndmask_b32_e32 v6, v227, v6, vcc
	v_cmp_le_i32_e32 vcc, v37, v238
	v_or_b32_e32 v37, 35, v2
	s_nop 0
	v_cndmask_b32_e32 v23, v227, v23, vcc
	v_cmp_le_i32_e32 vcc, v37, v238
	v_or_b32_e32 v37, 8, v2
	s_nop 0
	v_cndmask_b32_e32 v7, v227, v7, vcc
	v_cmp_le_i32_e32 vcc, v37, v238
	v_or_b32_e32 v37, 40, v2
	s_nop 0
	v_cndmask_b32_e32 v24, v227, v24, vcc
	v_cmp_le_i32_e32 vcc, v37, v238
	v_or_b32_e32 v37, 9, v2
	s_nop 0
	v_cndmask_b32_e32 v8, v227, v8, vcc
	v_cmp_le_i32_e32 vcc, v37, v238
	v_or_b32_e32 v37, 41, v2
	s_nop 0
	v_cndmask_b32_e32 v25, v227, v25, vcc
	v_cmp_le_i32_e32 vcc, v37, v238
	v_or_b32_e32 v37, 10, v2
	s_nop 0
	v_cndmask_b32_e32 v9, v227, v9, vcc
	v_cmp_le_i32_e32 vcc, v37, v238
	v_or_b32_e32 v37, 42, v2
	s_nop 0
	v_cndmask_b32_e32 v26, v227, v26, vcc
	v_cmp_le_i32_e32 vcc, v37, v238
	v_or_b32_e32 v37, 11, v2
	s_nop 0
	v_cndmask_b32_e32 v10, v227, v10, vcc
	v_cmp_le_i32_e32 vcc, v37, v238
	v_or_b32_e32 v37, 43, v2
	s_nop 0
	v_cndmask_b32_e32 v27, v227, v27, vcc
	v_cmp_le_i32_e32 vcc, v37, v238
	v_or_b32_e32 v37, 16, v2
	s_nop 0
	v_cndmask_b32_e32 v11, v227, v11, vcc
	v_cmp_le_i32_e32 vcc, v37, v238
	v_or_b32_e32 v37, 48, v2
	s_nop 0
	v_cndmask_b32_e32 v28, v227, v28, vcc
	v_cmp_le_i32_e32 vcc, v37, v238
	v_or_b32_e32 v37, 17, v2
	s_nop 0
	v_cndmask_b32_e32 v12, v227, v12, vcc
	v_cmp_le_i32_e32 vcc, v37, v238
	v_or_b32_e32 v37, 49, v2
	s_nop 0
	v_cndmask_b32_e32 v29, v227, v29, vcc
	v_cmp_le_i32_e32 vcc, v37, v238
	v_or_b32_e32 v37, 18, v2
	s_nop 0
	v_cndmask_b32_e32 v13, v227, v13, vcc
	v_cmp_le_i32_e32 vcc, v37, v238
	v_or_b32_e32 v37, 50, v2
	s_nop 0
	v_cndmask_b32_e32 v30, v227, v30, vcc
	v_cmp_le_i32_e32 vcc, v37, v238
	v_or_b32_e32 v37, 19, v2
	s_nop 0
	v_cndmask_b32_e32 v14, v227, v14, vcc
	v_cmp_le_i32_e32 vcc, v37, v238
	v_or_b32_e32 v37, 51, v2
	s_nop 0
	v_cndmask_b32_e32 v31, v227, v31, vcc
	v_cmp_le_i32_e32 vcc, v37, v238
	v_or_b32_e32 v37, 24, v2
	s_nop 0
	v_cndmask_b32_e32 v15, v227, v15, vcc
	v_cmp_le_i32_e32 vcc, v37, v238
	v_or_b32_e32 v37, 56, v2
	s_nop 0
	v_cndmask_b32_e32 v32, v227, v32, vcc
	v_cmp_le_i32_e32 vcc, v37, v238
	v_or_b32_e32 v37, 25, v2
	s_nop 0
	v_cndmask_b32_e32 v16, v227, v16, vcc
	v_cmp_le_i32_e32 vcc, v37, v238
	v_or_b32_e32 v37, 57, v2
	s_nop 0
	v_cndmask_b32_e32 v33, v227, v33, vcc
	v_cmp_le_i32_e32 vcc, v37, v238
	v_or_b32_e32 v37, 26, v2
	s_nop 0
	v_cndmask_b32_e32 v17, v227, v17, vcc
	v_cmp_le_i32_e32 vcc, v37, v238
	v_or_b32_e32 v37, 58, v2
	s_nop 0
	v_cndmask_b32_e32 v34, v227, v34, vcc
	v_cmp_le_i32_e32 vcc, v37, v238
	v_or_b32_e32 v37, 27, v2
	v_or_b32_e32 v2, 59, v2
	v_cndmask_b32_e32 v18, v227, v18, vcc
	v_cmp_le_i32_e32 vcc, v37, v238
	s_nop 1
	v_cndmask_b32_e32 v35, v227, v35, vcc
	v_cmp_le_i32_e32 vcc, v2, v238
	s_nop 1
	v_cndmask_b32_e32 v19, v227, v19, vcc

.LBB0_959:
	v_max_f32_e32 v16, v16, v16
	v_max_f32_e32 v17, 0, v16
	v_exp_f32_e64 v16, -v17
	v_cmp_gt_u32_e32 vcc, 32, v230
	s_and_saveexec_b64 s[2:3], vcc
	ds_write_b32 v235, v16
	s_or_b64 exec, exec, s[2:3]
	v_sub_f32_e32 v113, v113, v17
	v_sub_f32_e32 v112, v112, v17
	v_sub_f32_e32 v111, v111, v17
	v_sub_f32_e32 v110, v110, v17
	v_sub_f32_e32 v109, v109, v17
	v_sub_f32_e32 v108, v108, v17
	v_sub_f32_e32 v107, v107, v17
	v_sub_f32_e32 v106, v106, v17
	v_sub_f32_e32 v105, v105, v17
	v_sub_f32_e32 v104, v104, v17
	v_sub_f32_e32 v103, v103, v17
	v_sub_f32_e32 v102, v102, v17
	v_sub_f32_e32 v101, v101, v17
	v_sub_f32_e32 v100, v100, v17
	v_sub_f32_e32 v99, v99, v17
	v_sub_f32_e32 v98, v98, v17
	v_sub_f32_e32 v97, v97, v17
	v_sub_f32_e32 v96, v96, v17
	v_sub_f32_e32 v95, v95, v17
	v_sub_f32_e32 v94, v94, v17
	v_sub_f32_e32 v93, v93, v17
	v_sub_f32_e32 v92, v92, v17
	v_sub_f32_e32 v91, v91, v17
	v_sub_f32_e32 v90, v90, v17
	v_sub_f32_e32 v89, v89, v17
	v_sub_f32_e32 v88, v88, v17
	v_sub_f32_e32 v87, v87, v17
	v_sub_f32_e32 v86, v86, v17
	v_sub_f32_e32 v85, v85, v17
	v_sub_f32_e32 v84, v84, v17
	v_sub_f32_e32 v83, v83, v17
	v_sub_f32_e32 v82, v82, v17
	v_mul_f32_e32 v243, v243, v16
	s_branch .LBB0_953
	s_nop 0
	s_nop 0
	s_nop 0
	s_nop 0
	s_nop 0
	s_nop 0
	s_nop 0
	s_nop 0
	s_nop 0
	s_nop 0
	s_nop 0
	s_nop 0
	s_nop 0
	s_nop 0
	s_nop 0
